# P7 stage B: first four w_router vectors of each trip prefetched one trip ahead into v[238:253] (wrapping across batches)
# baseline (speedup 1.0000x reference)
; #define LAS __attribute__((address_space(3)))
; template <bool FAST>
; __device__ __forceinline__ void p7_route_t(Frame& F, const bool do_route) {
;     const float* mod = WSP(float, WS_MOD); const bf16_t* MIX = WSP(bf16_t, WS_MIX); bf16_t* X1 = WSP(bf16_t, WS_X1); unsigned char* H2 = WSP(unsigned char, WS_H2);
;     int* tok_e = WSP(int, WS_ROUTE); int* tok_rank = tok_e + M_LAT * TOPK; float* tok_gate = (float*)(tok_rank + M_LAT * TOPK); int* elist = (int*)(tok_gate + M_LAT * TOPK);
;     unsigned* cnt = WSP(unsigned, WS_CTL) + CW_CNT;
;     const int gw = F.bx * NWAVES + F.wave, NGW = F.G * NWAVES, rep = F.bx % RR;
;     LAS unsigned* lcnt = (LAS unsigned*)F.lds;
;     LAS float* hbuf = (LAS float*)(F.lds + 1024);
;     LAS float* part = (LAS float*)(F.lds + 1024 + 65536);
;     LAS float* lgb = (LAS float*)(F.lds + 1024 + 65536 + 32768);
;     LAS float* pvec = (LAS float*)(F.lds + 100352);
;     const int NIT = (M_LAT + NGW - 1) / NGW;
;     __syncthreads();
;     if (F.tid < 64) lcnt[F.tid] = 0u;
;     if (FAST) { const float* mr = mod + ((F.bx * NIT * 8) / T) * NMOD;
;         for (int c = 4 * F.tid; c < D; c += 4 * NTHR) {
;             *(LAS f32x4*)(pvec + c) = *(const f32x4*)(mr + 2 * D + c) * *(const f32x4*)(IN_NORMG + D + c);
;             *(LAS f32x4*)(pvec + D + c) = *(const f32x4*)(IN_NORMG + 2 * D + c) * (*(const f32x4*)(mr + 4 * D + c) + 1.0f);
;             *(LAS f32x4*)(pvec + 2 * D + c) = *(const f32x4*)(mr + 3 * D + c); } }
;     __syncthreads();
;     const int re = F.tid & 31;
;     ...
;             const int cg = F.lane >> 3, eq = F.lane & 7;
;             const float* wp = IN_WROUTER + (size_t)(256 * F.wave + cg) * NE + 4 * eq;
;             const LAS float* hp = hbuf + 256 * F.wave + cg;
; #pragma unroll 8
;             for (int it = 0; it < 32; ++it) { const f32x4 w4 = *(const f32x4*)(wp + (size_t)(8 * it) * NE);
.LBB0_787:
	s_or_b64 exec, exec, s[2:3]
	s_add_u32 s82, s96, 0x8ec00000
	s_addc_u32 s83, s97, 0
	s_add_u32 s86, s96, 0x8ec40000
	s_addc_u32 s87, s97, 0
	s_cmp_gt_i32 s85, 0
	s_cselect_b64 s[0:1], -1, 0
	s_mov_b32 s33, 0
	v_writelane_b32 v254, s0, 39
	s_cmp_lt_i32 s85, 1
	v_cmp_lt_u32_e64 s[4:5], 3, v1
	s_waitcnt lgkmcnt(0)
	s_barrier
	v_writelane_b32 v254, s1, 40
	s_cbranch_scc1 .LBB0_835
	s_add_u32 s84, s96, 0x82c00000
	s_addc_u32 s26, s97, 0
	s_add_u32 s88, s96, 0x8ac00000
	s_addc_u32 s89, s97, 0
	s_add_u32 s0, s96, 0x8ec80000
	v_writelane_b32 v254, s91, 41
	s_addc_u32 s1, s97, 0
	v_writelane_b32 v254, s0, 33
	v_mov_b32_e32 v35, 0
	v_lshlrev_b32_e32 v4, 3, v1
	v_writelane_b32 v254, s1, 34
	v_mov_b32_e32 v5, v35
	v_lshl_add_u64 v[4:5], s[96:97], 0, v[4:5]
	s_mov_b64 s[0:1], 0x7ac00000
	v_readlane_b32 s8, v254, 17
	v_lshl_add_u64 v[36:37], v[4:5], 0, s[0:1]
	v_lshlrev_b32_e32 v4, 4, v1
	v_mov_b32_e32 v5, v35
	v_readlane_b32 s9, v254, 18
	v_readlane_b32 s16, v254, 25
	s_add_i32 s0, 0, 0x18800
	v_lshl_add_u64 v[38:39], s[8:9], 0, v[4:5]
	v_or_b32_e32 v3, 0x400, v4
	v_or_b32_e32 v5, 0x800, v4
	v_or_b32_e32 v6, 0xc00, v4
	v_or_b32_e32 v7, 0x1000, v4
	v_or_b32_e32 v8, 0x1400, v4
	v_or_b32_e32 v9, 0x1800, v4
	v_or_b32_e32 v10, 0x1c00, v4
	v_add_u32_e32 v78, s0, v4
	v_add_u32_e32 v79, s0, v3
	v_add_u32_e32 v80, s0, v5
	v_add_u32_e32 v81, s0, v6
	v_add_u32_e32 v82, s0, v7
	v_add_u32_e32 v83, s0, v8
	v_add_u32_e32 v84, s0, v9
	v_add_u32_e32 v85, s0, v10
	s_add_i32 s0, 0, 0x1a800
	v_readlane_b32 s16, v254, 35
	v_add_u32_e32 v86, s0, v4
	s_add_i32 s1, 0, 0x1c800
	s_lshl_b32 s3, s16, 13
	v_add_u32_e32 v89, s0, v3
	v_add_u32_e32 v91, s0, v5
	v_add_u32_e32 v93, s0, v6
	v_add_u32_e32 v95, s0, v7
	v_add_u32_e32 v97, s0, v8
	v_add_u32_e32 v99, s0, v9
	v_add_u32_e32 v101, s0, v10
	s_lshl_b32 s0, s16, 12
	s_add_i32 s3, s3, 0
	v_add_u32_e32 v90, s1, v3
	v_and_b32_e32 v3, 8, v0
	s_add_i32 s0, s0, 0
	v_and_b32_e32 v2, 31, v0
	v_add_u32_e32 v87, s1, v4
	v_add_u32_e32 v88, s3, v4
	v_cmp_eq_u32_e64 s[6:7], 0, v3
	v_and_b32_e32 v3, 0x70, v4
	v_lshlrev_b32_e32 v4, 6, v0
	s_add_i32 s0, s0, 0x10400
	v_lshlrev_b32_e32 v2, 2, v2
	v_add_u32_e32 v94, s1, v6
	v_add_u32_e32 v96, s1, v7
	v_add_u32_e32 v98, s1, v8
	v_lshrrev_b32_e32 v6, 3, v1
	v_and_b32_e32 v7, 0xc00, v4
	v_add_u32_e32 v8, s0, v3
	v_and_b32_e32 v4, 0xe0, v0
	v_mov_b32_e32 v3, v35
	s_add_i32 s2, 0, 0x18400
	v_add_u32_e32 v92, s1, v5
	v_add_u32_e32 v100, s1, v9
	v_add_u32_e32 v102, s1, v10
	v_lshl_add_u64 v[40:41], s[48:49], 0, v[2:3]
	v_lshlrev_b32_e32 v3, 2, v4
	v_lshl_or_b32 v4, s16, 8, v6
	v_mov_b32_e32 v5, v35
	s_lshl_b32 s1, s16, 10
	v_add3_u32 v103, s2, v2, v3
	v_lshlrev_b64 v[4:5], 7, v[4:5]
	v_and_b32_e32 v3, 7, v0
	s_add_i32 s1, s1, 0
	s_movk_i32 s0, 0x100
	v_lshl_or_b32 v4, v3, 4, v4
	v_lshl_add_u32 v3, v6, 2, s1
	v_cmp_gt_u32_e64 s[8:9], s0, v0
	s_lshl_b32 s0, s16, 7
	v_add_u32_e32 v104, 0x400, v3
	v_lshlrev_b32_e32 v3, 2, v0
	s_movk_i32 s1, 0x380
	v_readlane_b32 s10, v254, 19
	v_readlane_b32 s11, v254, 20
	v_readlane_b32 s12, v254, 21
	v_readlane_b32 s13, v254, 22
	v_readlane_b32 s14, v254, 23
	v_readlane_b32 s15, v254, 24
	v_and_or_b32 v2, v3, s1, v2
	s_add_i32 s0, s0, 0
	v_lshlrev_b32_e32 v34, 2, v1
	s_movk_i32 s92, 0x1000
	v_cmp_eq_u32_e64 s[10:11], 0, v1
	v_cmp_eq_u32_e64 s[12:13], 1, v1
	v_cmp_eq_u32_e64 s[14:15], 2, v1
	v_lshl_add_u64 v[42:43], s[46:47], 0, v[4:5]
	v_add_u32_e32 v105, 0, v2
	v_mov_b32_e32 v106, 0x358637bd
	v_add_u32_e32 v107, v8, v7
	s_add_i32 s0, s0, 0x18400
	v_mov_b32_e32 v108, 0xff61b1e6
	v_mov_b32_e32 v109, 1
	v_readlane_b32 s17, v254, 26
	v_readlane_b32 s18, v254, 27
	v_readlane_b32 s19, v254, 28
	v_readlane_b32 s20, v254, 29
	v_readlane_b32 s21, v254, 30
	v_readlane_b32 s22, v254, 31
	v_readlane_b32 s23, v254, 32
	v_writelane_b32 v254, s0, 42
	global_load_dwordx4 v[238:241], v[42:43], off
	global_load_dwordx4 v[242:245], v[42:43], off offset:1024
	global_load_dwordx4 v[246:249], v[42:43], off offset:2048
	global_load_dwordx4 v[250:253], v[42:43], off offset:3072
	s_branch .LBB0_790

; #define LAS __attribute__((address_space(3)))
; template <bool FAST>
; __device__ __forceinline__ void p7_route_t(Frame& F, const bool do_route) {
;     ...
;             const int cg = F.lane >> 3, eq = F.lane & 7;
;             const float* wp = IN_WROUTER + (size_t)(256 * F.wave + cg) * NE + 4 * eq;
;             const LAS float* hp = hbuf + 256 * F.wave + cg;
; #pragma unroll 8
;             for (int it = 0; it < 32; ++it) { const f32x4 w4 = *(const f32x4*)(wp + (size_t)(8 * it) * NE);
; #pragma unroll
;                 for (int r = 0; r < 8; ++r) acc[r] += hp[r * D + 8 * it] * w4; }
.LBB0_825:
	v_mov_b64_e32 v[56:57], v[238:239]
	v_mov_b64_e32 v[58:59], v[240:241]
	v_mov_b64_e32 v[60:61], v[242:243]
	v_mov_b64_e32 v[62:63], v[244:245]
	v_mov_b64_e32 v[64:65], v[246:247]
	v_mov_b64_e32 v[66:67], v[248:249]
	v_mov_b64_e32 v[68:69], v[250:251]
	v_mov_b64_e32 v[70:71], v[252:253]
	s_add_u32 s100, s16, 0x2000
	s_and_b32 s100, s100, 0x7fff
	s_mov_b32 s101, 0
	v_lshl_add_u64 v[176:177], v[42:43], 0, s[100:101]
	v_lshl_add_u64 v[46:47], v[42:43], 0, s[16:17]
	ds_read2_b32 v[44:45], v54 offset1:8
	v_add_u32_e32 v55, 0x2000, v54
	ds_read2_b32 v[48:49], v54 offset0:16 offset1:24
	ds_read2_b32 v[50:51], v54 offset0:32 offset1:40
	ds_read2_b32 v[52:53], v54 offset0:48 offset1:56
	global_load_dwordx4 v[238:241], v[176:177], off
	v_add_u32_e32 v72, 0x4000, v54
	v_add_u32_e32 v73, 0x6000, v54
	v_add_u32_e32 v74, 0x8000, v54
	v_add_u32_e32 v75, 0xa000, v54
	v_add_u32_e32 v110, 0xc000, v54
	v_add_u32_e32 v111, 0xe000, v54
	ds_read2_b32 v[76:77], v55 offset1:8
	ds_read2_b32 v[122:123], v72 offset1:8
	ds_read2_b32 v[124:125], v73 offset1:8
	ds_read2_b32 v[126:127], v74 offset1:8
	ds_read2_b32 v[128:129], v75 offset1:8
	ds_read2_b32 v[130:131], v110 offset1:8
	ds_read2_b32 v[132:133], v111 offset1:8
	global_load_dwordx4 v[242:245], v[176:177], off offset:1024
	ds_read2_b32 v[134:135], v55 offset0:16 offset1:24
	ds_read2_b32 v[136:137], v72 offset0:16 offset1:24
	ds_read2_b32 v[138:139], v73 offset0:16 offset1:24
	ds_read2_b32 v[140:141], v74 offset0:16 offset1:24
	ds_read2_b32 v[142:143], v75 offset0:16 offset1:24
	ds_read2_b32 v[144:145], v110 offset0:16 offset1:24
	ds_read2_b32 v[146:147], v111 offset0:16 offset1:24
	global_load_dwordx4 v[246:249], v[176:177], off offset:2048
	global_load_dwordx4 v[250:253], v[176:177], off offset:3072
	v_add_co_u32_e32 v46, vcc, s92, v46
	ds_read2_b32 v[148:149], v55 offset0:32 offset1:40
	ds_read2_b32 v[150:151], v72 offset0:32 offset1:40
	ds_read2_b32 v[152:153], v73 offset0:32 offset1:40
	ds_read2_b32 v[154:155], v74 offset0:32 offset1:40
	ds_read2_b32 v[156:157], v75 offset0:32 offset1:40
	ds_read2_b32 v[158:159], v110 offset0:32 offset1:40
	ds_read2_b32 v[160:161], v111 offset0:32 offset1:40
	ds_read2_b32 v[162:163], v55 offset0:48 offset1:56
	ds_read2_b32 v[164:165], v72 offset0:48 offset1:56
	ds_read2_b32 v[166:167], v73 offset0:48 offset1:56
	ds_read2_b32 v[168:169], v74 offset0:48 offset1:56
	ds_read2_b32 v[170:171], v75 offset0:48 offset1:56
	ds_read2_b32 v[172:173], v110 offset0:48 offset1:56
	ds_read2_b32 v[174:175], v111 offset0:48 offset1:56
	v_addc_co_u32_e32 v47, vcc, 0, v47, vcc
	global_load_dwordx4 v[72:75], v[46:47], off
	global_load_dwordx4 v[110:113], v[46:47], off offset:1024
	global_load_dwordx4 v[114:117], v[46:47], off offset:2048
	global_load_dwordx4 v[118:121], v[46:47], off offset:3072
	s_waitcnt lgkmcnt(14)
	v_mov_b32_e32 v46, v45
	v_mov_b32_e32 v182, v77
	v_mov_b32_e32 v184, v123
	v_mov_b32_e32 v186, v125
	v_mov_b32_e32 v188, v127
	v_mov_b32_e32 v190, v129
	v_mov_b32_e32 v192, v131
	v_mov_b32_e32 v194, v133
	v_mov_b32_e32 v176, v49
	v_mov_b32_e32 v196, v135
	v_mov_b32_e32 v198, v137
	v_mov_b32_e32 v200, v139
	v_mov_b32_e32 v202, v141
	v_mov_b32_e32 v204, v143
	v_mov_b32_e32 v206, v145
	v_mov_b32_e32 v208, v147
	v_mov_b32_e32 v178, v51
	s_waitcnt lgkmcnt(13)
	v_mov_b32_e32 v210, v149
	s_waitcnt lgkmcnt(12)
	v_mov_b32_e32 v212, v151
	s_waitcnt lgkmcnt(11)
	v_mov_b32_e32 v214, v153
	s_waitcnt lgkmcnt(10)
	v_mov_b32_e32 v216, v155
	s_waitcnt lgkmcnt(9)
	v_mov_b32_e32 v218, v157
	s_waitcnt lgkmcnt(8)
	v_mov_b32_e32 v220, v159
	s_waitcnt lgkmcnt(7)
	v_mov_b32_e32 v222, v161
	s_add_u32 s16, s16, 0x2000
	s_addc_u32 s17, s17, 0
	v_mov_b32_e32 v180, v53
	s_waitcnt lgkmcnt(6)
	v_mov_b32_e32 v224, v163
	s_waitcnt lgkmcnt(5)
	v_mov_b32_e32 v226, v165
	s_waitcnt lgkmcnt(4)
	v_mov_b32_e32 v228, v167
	s_waitcnt lgkmcnt(3)
	v_mov_b32_e32 v230, v169
	s_waitcnt lgkmcnt(2)
	v_mov_b32_e32 v232, v171
	s_waitcnt lgkmcnt(1)
	v_mov_b32_e32 v234, v173
	s_waitcnt lgkmcnt(0)
	v_mov_b32_e32 v236, v175
	v_add_u32_e32 v54, 0x100, v54
	s_cmpk_lg_u32 s16, 0x8000
	v_pk_fma_f32 v[30:31], v[56:57], v[44:45], v[30:31] op_sel_hi:[1,0,1]
	v_pk_fma_f32 v[32:33], v[58:59], v[44:45], v[32:33] op_sel_hi:[1,0,1]
	v_pk_fma_f32 v[26:27], v[56:57], v[76:77], v[26:27] op_sel_hi:[1,0,1]
	v_pk_fma_f32 v[28:29], v[58:59], v[76:77], v[28:29] op_sel_hi:[1,0,1]
	v_pk_fma_f32 v[22:23], v[56:57], v[122:123], v[22:23] op_sel_hi:[1,0,1]
	v_pk_fma_f32 v[24:25], v[58:59], v[122:123], v[24:25] op_sel_hi:[1,0,1]
	v_pk_fma_f32 v[18:19], v[56:57], v[124:125], v[18:19] op_sel_hi:[1,0,1]
	v_pk_fma_f32 v[20:21], v[58:59], v[124:125], v[20:21] op_sel_hi:[1,0,1]
	v_pk_fma_f32 v[14:15], v[56:57], v[126:127], v[14:15] op_sel_hi:[1,0,1]
	v_pk_fma_f32 v[16:17], v[58:59], v[126:127], v[16:17] op_sel_hi:[1,0,1]
	v_pk_fma_f32 v[10:11], v[56:57], v[128:129], v[10:11] op_sel_hi:[1,0,1]
	v_pk_fma_f32 v[12:13], v[58:59], v[128:129], v[12:13] op_sel_hi:[1,0,1]
	v_pk_fma_f32 v[6:7], v[56:57], v[130:131], v[6:7] op_sel_hi:[1,0,1]
	v_pk_fma_f32 v[8:9], v[58:59], v[130:131], v[8:9] op_sel_hi:[1,0,1]
	v_pk_fma_f32 v[2:3], v[56:57], v[132:133], v[2:3] op_sel_hi:[1,0,1]
	v_pk_fma_f32 v[4:5], v[58:59], v[132:133], v[4:5] op_sel_hi:[1,0,1]
	v_pk_fma_f32 v[30:31], v[60:61], v[46:47], v[30:31] op_sel_hi:[1,0,1]
	v_pk_fma_f32 v[32:33], v[62:63], v[46:47], v[32:33] op_sel_hi:[1,0,1]
	v_pk_fma_f32 v[26:27], v[60:61], v[182:183], v[26:27] op_sel_hi:[1,0,1]
	v_pk_fma_f32 v[28:29], v[62:63], v[182:183], v[28:29] op_sel_hi:[1,0,1]
	v_pk_fma_f32 v[22:23], v[60:61], v[184:185], v[22:23] op_sel_hi:[1,0,1]
	v_pk_fma_f32 v[24:25], v[62:63], v[184:185], v[24:25] op_sel_hi:[1,0,1]
; template <bool FAST>
; __device__ __forceinline__ void p7_route_t(Frame& F, const bool do_route) {
;     ...
;             for (int it = 0; it < 32; ++it) { const f32x4 w4 = *(const f32x4*)(wp + (size_t)(8 * it) * NE);
; #pragma unroll
;                 for (int r = 0; r < 8; ++r) acc[r] += hp[r * D + 8 * it] * w4; }
	v_pk_fma_f32 v[18:19], v[60:61], v[186:187], v[18:19] op_sel_hi:[1,0,1]
	v_pk_fma_f32 v[20:21], v[62:63], v[186:187], v[20:21] op_sel_hi:[1,0,1]
	v_pk_fma_f32 v[14:15], v[60:61], v[188:189], v[14:15] op_sel_hi:[1,0,1]
	v_pk_fma_f32 v[16:17], v[62:63], v[188:189], v[16:17] op_sel_hi:[1,0,1]
	v_pk_fma_f32 v[10:11], v[60:61], v[190:191], v[10:11] op_sel_hi:[1,0,1]
	v_pk_fma_f32 v[12:13], v[62:63], v[190:191], v[12:13] op_sel_hi:[1,0,1]
	v_pk_fma_f32 v[6:7], v[60:61], v[192:193], v[6:7] op_sel_hi:[1,0,1]
	v_pk_fma_f32 v[8:9], v[62:63], v[192:193], v[8:9] op_sel_hi:[1,0,1]
	v_pk_fma_f32 v[2:3], v[60:61], v[194:195], v[2:3] op_sel_hi:[1,0,1]
	v_pk_fma_f32 v[4:5], v[62:63], v[194:195], v[4:5] op_sel_hi:[1,0,1]
	v_pk_fma_f32 v[32:33], v[66:67], v[48:49], v[32:33] op_sel_hi:[1,0,1]
	v_pk_fma_f32 v[30:31], v[64:65], v[48:49], v[30:31] op_sel_hi:[1,0,1]
	v_pk_fma_f32 v[28:29], v[66:67], v[134:135], v[28:29] op_sel_hi:[1,0,1]
	v_pk_fma_f32 v[26:27], v[64:65], v[134:135], v[26:27] op_sel_hi:[1,0,1]
	v_pk_fma_f32 v[24:25], v[66:67], v[136:137], v[24:25] op_sel_hi:[1,0,1]
	v_pk_fma_f32 v[22:23], v[64:65], v[136:137], v[22:23] op_sel_hi:[1,0,1]
	v_pk_fma_f32 v[20:21], v[66:67], v[138:139], v[20:21] op_sel_hi:[1,0,1]
	v_pk_fma_f32 v[18:19], v[64:65], v[138:139], v[18:19] op_sel_hi:[1,0,1]
	v_pk_fma_f32 v[16:17], v[66:67], v[140:141], v[16:17] op_sel_hi:[1,0,1]
	v_pk_fma_f32 v[14:15], v[64:65], v[140:141], v[14:15] op_sel_hi:[1,0,1]
	v_pk_fma_f32 v[12:13], v[66:67], v[142:143], v[12:13] op_sel_hi:[1,0,1]
	v_pk_fma_f32 v[10:11], v[64:65], v[142:143], v[10:11] op_sel_hi:[1,0,1]
	v_pk_fma_f32 v[8:9], v[66:67], v[144:145], v[8:9] op_sel_hi:[1,0,1]
	v_pk_fma_f32 v[6:7], v[64:65], v[144:145], v[6:7] op_sel_hi:[1,0,1]
	v_pk_fma_f32 v[4:5], v[66:67], v[146:147], v[4:5] op_sel_hi:[1,0,1]
	v_pk_fma_f32 v[2:3], v[64:65], v[146:147], v[2:3] op_sel_hi:[1,0,1]
	v_pk_fma_f32 v[30:31], v[68:69], v[176:177], v[30:31] op_sel_hi:[1,0,1]
	v_pk_fma_f32 v[32:33], v[70:71], v[176:177], v[32:33] op_sel_hi:[1,0,1]
	v_pk_fma_f32 v[26:27], v[68:69], v[196:197], v[26:27] op_sel_hi:[1,0,1]
	v_pk_fma_f32 v[28:29], v[70:71], v[196:197], v[28:29] op_sel_hi:[1,0,1]
	v_pk_fma_f32 v[22:23], v[68:69], v[198:199], v[22:23] op_sel_hi:[1,0,1]
	v_pk_fma_f32 v[24:25], v[70:71], v[198:199], v[24:25] op_sel_hi:[1,0,1]
	v_pk_fma_f32 v[18:19], v[68:69], v[200:201], v[18:19] op_sel_hi:[1,0,1]
	v_pk_fma_f32 v[20:21], v[70:71], v[200:201], v[20:21] op_sel_hi:[1,0,1]
	v_pk_fma_f32 v[14:15], v[68:69], v[202:203], v[14:15] op_sel_hi:[1,0,1]
	v_pk_fma_f32 v[16:17], v[70:71], v[202:203], v[16:17] op_sel_hi:[1,0,1]
	v_pk_fma_f32 v[10:11], v[68:69], v[204:205], v[10:11] op_sel_hi:[1,0,1]
	v_pk_fma_f32 v[12:13], v[70:71], v[204:205], v[12:13] op_sel_hi:[1,0,1]
	v_pk_fma_f32 v[6:7], v[68:69], v[206:207], v[6:7] op_sel_hi:[1,0,1]
	v_pk_fma_f32 v[8:9], v[70:71], v[206:207], v[8:9] op_sel_hi:[1,0,1]
	v_pk_fma_f32 v[2:3], v[68:69], v[208:209], v[2:3] op_sel_hi:[1,0,1]
	v_pk_fma_f32 v[4:5], v[70:71], v[208:209], v[4:5] op_sel_hi:[1,0,1]
	s_waitcnt vmcnt(3)
	v_pk_fma_f32 v[32:33], v[74:75], v[50:51], v[32:33] op_sel_hi:[1,0,1]
	v_pk_fma_f32 v[30:31], v[72:73], v[50:51], v[30:31] op_sel_hi:[1,0,1]
	v_pk_fma_f32 v[28:29], v[74:75], v[148:149], v[28:29] op_sel_hi:[1,0,1]
	v_pk_fma_f32 v[26:27], v[72:73], v[148:149], v[26:27] op_sel_hi:[1,0,1]
	v_pk_fma_f32 v[24:25], v[74:75], v[150:151], v[24:25] op_sel_hi:[1,0,1]
	v_pk_fma_f32 v[22:23], v[72:73], v[150:151], v[22:23] op_sel_hi:[1,0,1]
	v_pk_fma_f32 v[20:21], v[74:75], v[152:153], v[20:21] op_sel_hi:[1,0,1]
	v_pk_fma_f32 v[18:19], v[72:73], v[152:153], v[18:19] op_sel_hi:[1,0,1]
	v_pk_fma_f32 v[16:17], v[74:75], v[154:155], v[16:17] op_sel_hi:[1,0,1]
	v_pk_fma_f32 v[14:15], v[72:73], v[154:155], v[14:15] op_sel_hi:[1,0,1]
	v_pk_fma_f32 v[12:13], v[74:75], v[156:157], v[12:13] op_sel_hi:[1,0,1]
	v_pk_fma_f32 v[10:11], v[72:73], v[156:157], v[10:11] op_sel_hi:[1,0,1]
	v_pk_fma_f32 v[8:9], v[74:75], v[158:159], v[8:9] op_sel_hi:[1,0,1]
	v_pk_fma_f32 v[6:7], v[72:73], v[158:159], v[6:7] op_sel_hi:[1,0,1]
	v_pk_fma_f32 v[4:5], v[74:75], v[160:161], v[4:5] op_sel_hi:[1,0,1]
	v_pk_fma_f32 v[2:3], v[72:73], v[160:161], v[2:3] op_sel_hi:[1,0,1]
	s_waitcnt vmcnt(2)
	v_pk_fma_f32 v[32:33], v[112:113], v[178:179], v[32:33] op_sel_hi:[1,0,1]
	v_pk_fma_f32 v[30:31], v[110:111], v[178:179], v[30:31] op_sel_hi:[1,0,1]
	v_pk_fma_f32 v[28:29], v[112:113], v[210:211], v[28:29] op_sel_hi:[1,0,1]
	v_pk_fma_f32 v[26:27], v[110:111], v[210:211], v[26:27] op_sel_hi:[1,0,1]
	v_pk_fma_f32 v[24:25], v[112:113], v[212:213], v[24:25] op_sel_hi:[1,0,1]
	v_pk_fma_f32 v[22:23], v[110:111], v[212:213], v[22:23] op_sel_hi:[1,0,1]
	v_pk_fma_f32 v[20:21], v[112:113], v[214:215], v[20:21] op_sel_hi:[1,0,1]
	v_pk_fma_f32 v[18:19], v[110:111], v[214:215], v[18:19] op_sel_hi:[1,0,1]
	v_pk_fma_f32 v[16:17], v[112:113], v[216:217], v[16:17] op_sel_hi:[1,0,1]
	v_pk_fma_f32 v[14:15], v[110:111], v[216:217], v[14:15] op_sel_hi:[1,0,1]
	v_pk_fma_f32 v[12:13], v[112:113], v[218:219], v[12:13] op_sel_hi:[1,0,1]
	v_pk_fma_f32 v[10:11], v[110:111], v[218:219], v[10:11] op_sel_hi:[1,0,1]
	v_pk_fma_f32 v[8:9], v[112:113], v[220:221], v[8:9] op_sel_hi:[1,0,1]
	v_pk_fma_f32 v[6:7], v[110:111], v[220:221], v[6:7] op_sel_hi:[1,0,1]
	v_pk_fma_f32 v[4:5], v[112:113], v[222:223], v[4:5] op_sel_hi:[1,0,1]
	v_pk_fma_f32 v[2:3], v[110:111], v[222:223], v[2:3] op_sel_hi:[1,0,1]
	s_waitcnt vmcnt(1)
; #define LAS __attribute__((address_space(3)))
; template <int CTRL> __device__ __forceinline__ float dpp_add(float x) { return x + __builtin_bit_cast(float, __builtin_amdgcn_update_dpp(0, __builtin_bit_cast(int, x), CTRL, 0xF, 0xF, true)); }
; template <bool FAST>
; __device__ __forceinline__ void p7_route_t(Frame& F, const bool do_route) {
;     ...
;                 for (int r = 0; r < 8; ++r) acc[r] += hp[r * D + 8 * it] * w4; }
; #pragma unroll
;             for (int r = 0; r < 8; ++r) { acc[r].x = dpp_add<0x128>(acc[r].x); acc[r].y = dpp_add<0x128>(acc[r].y); acc[r].z = dpp_add<0x128>(acc[r].z); acc[r].w = dpp_add<0x128>(acc[r].w); }
;             if (!(cg & 1)) {
; #pragma unroll
;                 for (int r = 0; r < 8; ++r) *(LAS f32x4*)(part + ((F.wave * 4 + (cg >> 1)) * 8 + r) * 32 + 4 * eq) = acc[r]; }
	v_pk_fma_f32 v[32:33], v[116:117], v[52:53], v[32:33] op_sel_hi:[1,0,1]
	v_pk_fma_f32 v[30:31], v[114:115], v[52:53], v[30:31] op_sel_hi:[1,0,1]
	v_pk_fma_f32 v[28:29], v[116:117], v[162:163], v[28:29] op_sel_hi:[1,0,1]
	v_pk_fma_f32 v[26:27], v[114:115], v[162:163], v[26:27] op_sel_hi:[1,0,1]
	v_pk_fma_f32 v[24:25], v[116:117], v[164:165], v[24:25] op_sel_hi:[1,0,1]
	v_pk_fma_f32 v[22:23], v[114:115], v[164:165], v[22:23] op_sel_hi:[1,0,1]
	v_pk_fma_f32 v[20:21], v[116:117], v[166:167], v[20:21] op_sel_hi:[1,0,1]
	v_pk_fma_f32 v[18:19], v[114:115], v[166:167], v[18:19] op_sel_hi:[1,0,1]
	v_pk_fma_f32 v[16:17], v[116:117], v[168:169], v[16:17] op_sel_hi:[1,0,1]
	v_pk_fma_f32 v[14:15], v[114:115], v[168:169], v[14:15] op_sel_hi:[1,0,1]
	v_pk_fma_f32 v[12:13], v[116:117], v[170:171], v[12:13] op_sel_hi:[1,0,1]
	v_pk_fma_f32 v[10:11], v[114:115], v[170:171], v[10:11] op_sel_hi:[1,0,1]
	v_pk_fma_f32 v[8:9], v[116:117], v[172:173], v[8:9] op_sel_hi:[1,0,1]
	v_pk_fma_f32 v[6:7], v[114:115], v[172:173], v[6:7] op_sel_hi:[1,0,1]
	v_pk_fma_f32 v[4:5], v[116:117], v[174:175], v[4:5] op_sel_hi:[1,0,1]
	v_pk_fma_f32 v[2:3], v[114:115], v[174:175], v[2:3] op_sel_hi:[1,0,1]
	s_waitcnt vmcnt(0)
	v_pk_fma_f32 v[32:33], v[120:121], v[180:181], v[32:33] op_sel_hi:[1,0,1]
	v_pk_fma_f32 v[30:31], v[118:119], v[180:181], v[30:31] op_sel_hi:[1,0,1]
	v_pk_fma_f32 v[28:29], v[120:121], v[224:225], v[28:29] op_sel_hi:[1,0,1]
	v_pk_fma_f32 v[26:27], v[118:119], v[224:225], v[26:27] op_sel_hi:[1,0,1]
	v_pk_fma_f32 v[24:25], v[120:121], v[226:227], v[24:25] op_sel_hi:[1,0,1]
	v_pk_fma_f32 v[22:23], v[118:119], v[226:227], v[22:23] op_sel_hi:[1,0,1]
	v_pk_fma_f32 v[20:21], v[120:121], v[228:229], v[20:21] op_sel_hi:[1,0,1]
	v_pk_fma_f32 v[18:19], v[118:119], v[228:229], v[18:19] op_sel_hi:[1,0,1]
	v_pk_fma_f32 v[16:17], v[120:121], v[230:231], v[16:17] op_sel_hi:[1,0,1]
	v_pk_fma_f32 v[14:15], v[118:119], v[230:231], v[14:15] op_sel_hi:[1,0,1]
	v_pk_fma_f32 v[12:13], v[120:121], v[232:233], v[12:13] op_sel_hi:[1,0,1]
	v_pk_fma_f32 v[10:11], v[118:119], v[232:233], v[10:11] op_sel_hi:[1,0,1]
	v_pk_fma_f32 v[8:9], v[120:121], v[234:235], v[8:9] op_sel_hi:[1,0,1]
	v_pk_fma_f32 v[6:7], v[118:119], v[234:235], v[6:7] op_sel_hi:[1,0,1]
	v_pk_fma_f32 v[4:5], v[120:121], v[236:237], v[4:5] op_sel_hi:[1,0,1]
	v_pk_fma_f32 v[2:3], v[118:119], v[236:237], v[2:3] op_sel_hi:[1,0,1]
	s_cbranch_scc1 .LBB0_825
	v_mov_b32_dpp v72, v30 row_ror:8 row_mask:0xf bank_mask:0xf bound_ctrl:1
	v_mov_b32_dpp v73, v31 row_ror:8 row_mask:0xf bank_mask:0xf bound_ctrl:1
	v_mov_b32_dpp v74, v32 row_ror:8 row_mask:0xf bank_mask:0xf bound_ctrl:1
	v_mov_b32_dpp v75, v33 row_ror:8 row_mask:0xf bank_mask:0xf bound_ctrl:1
	v_mov_b32_dpp v68, v26 row_ror:8 row_mask:0xf bank_mask:0xf bound_ctrl:1
	v_mov_b32_dpp v69, v27 row_ror:8 row_mask:0xf bank_mask:0xf bound_ctrl:1
	v_mov_b32_dpp v70, v28 row_ror:8 row_mask:0xf bank_mask:0xf bound_ctrl:1
	v_mov_b32_dpp v71, v29 row_ror:8 row_mask:0xf bank_mask:0xf bound_ctrl:1
	v_mov_b32_dpp v64, v22 row_ror:8 row_mask:0xf bank_mask:0xf bound_ctrl:1
	v_mov_b32_dpp v65, v23 row_ror:8 row_mask:0xf bank_mask:0xf bound_ctrl:1
	v_mov_b32_dpp v66, v24 row_ror:8 row_mask:0xf bank_mask:0xf bound_ctrl:1
	v_mov_b32_dpp v67, v25 row_ror:8 row_mask:0xf bank_mask:0xf bound_ctrl:1
	v_mov_b32_dpp v60, v18 row_ror:8 row_mask:0xf bank_mask:0xf bound_ctrl:1
	v_mov_b32_dpp v61, v19 row_ror:8 row_mask:0xf bank_mask:0xf bound_ctrl:1
	v_mov_b32_dpp v62, v20 row_ror:8 row_mask:0xf bank_mask:0xf bound_ctrl:1
	v_mov_b32_dpp v63, v21 row_ror:8 row_mask:0xf bank_mask:0xf bound_ctrl:1
	v_mov_b32_dpp v56, v14 row_ror:8 row_mask:0xf bank_mask:0xf bound_ctrl:1
	v_mov_b32_dpp v57, v15 row_ror:8 row_mask:0xf bank_mask:0xf bound_ctrl:1
	v_mov_b32_dpp v58, v16 row_ror:8 row_mask:0xf bank_mask:0xf bound_ctrl:1
	v_mov_b32_dpp v59, v17 row_ror:8 row_mask:0xf bank_mask:0xf bound_ctrl:1
	v_mov_b32_dpp v52, v10 row_ror:8 row_mask:0xf bank_mask:0xf bound_ctrl:1
	v_mov_b32_dpp v53, v11 row_ror:8 row_mask:0xf bank_mask:0xf bound_ctrl:1
	v_mov_b32_dpp v54, v12 row_ror:8 row_mask:0xf bank_mask:0xf bound_ctrl:1
	v_mov_b32_dpp v55, v13 row_ror:8 row_mask:0xf bank_mask:0xf bound_ctrl:1
	v_mov_b32_dpp v48, v6 row_ror:8 row_mask:0xf bank_mask:0xf bound_ctrl:1
	v_mov_b32_dpp v49, v7 row_ror:8 row_mask:0xf bank_mask:0xf bound_ctrl:1
	v_mov_b32_dpp v50, v8 row_ror:8 row_mask:0xf bank_mask:0xf bound_ctrl:1
	v_mov_b32_dpp v51, v9 row_ror:8 row_mask:0xf bank_mask:0xf bound_ctrl:1
	v_mov_b32_dpp v44, v2 row_ror:8 row_mask:0xf bank_mask:0xf bound_ctrl:1
	v_mov_b32_dpp v45, v3 row_ror:8 row_mask:0xf bank_mask:0xf bound_ctrl:1
	v_mov_b32_dpp v46, v4 row_ror:8 row_mask:0xf bank_mask:0xf bound_ctrl:1
	v_mov_b32_dpp v47, v5 row_ror:8 row_mask:0xf bank_mask:0xf bound_ctrl:1
	s_and_saveexec_b64 s[2:3], s[6:7]
	s_cbranch_execz .LBB0_828
	v_pk_add_f32 v[32:33], v[32:33], v[74:75]
	v_pk_add_f32 v[30:31], v[30:31], v[72:73]
	v_pk_add_f32 v[28:29], v[28:29], v[70:71]
	v_pk_add_f32 v[26:27], v[26:27], v[68:69]
	v_pk_add_f32 v[24:25], v[24:25], v[66:67]
	v_pk_add_f32 v[22:23], v[22:23], v[64:65]
	v_pk_add_f32 v[20:21], v[20:21], v[62:63]
	v_pk_add_f32 v[18:19], v[18:19], v[60:61]
	v_pk_add_f32 v[16:17], v[16:17], v[58:59]
	v_pk_add_f32 v[14:15], v[14:15], v[56:57]
	v_pk_add_f32 v[12:13], v[12:13], v[54:55]
	v_pk_add_f32 v[10:11], v[10:11], v[52:53]
	v_pk_add_f32 v[8:9], v[8:9], v[50:51]
	v_pk_add_f32 v[6:7], v[6:7], v[48:49]
	v_pk_add_f32 v[4:5], v[4:5], v[46:47]
	v_pk_add_f32 v[2:3], v[2:3], v[44:45]
	ds_write_b128 v107, v[30:33]
	ds_write_b128 v107, v[26:29] offset:128
	ds_write_b128 v107, v[22:25] offset:256
	ds_write_b128 v107, v[18:21] offset:384
	ds_write_b128 v107, v[14:17] offset:512
	ds_write_b128 v107, v[10:13] offset:640
	ds_write_b128 v107, v[6:9] offset:768
	ds_write_b128 v107, v[2:5] offset:896
; template <bool FAST>
; __device__ __forceinline__ void p7_route_t(Frame& F, const bool do_route) {
;     ...
;         __syncthreads();
;         if (F.tid < 256) { const int r = F.tid >> 5; float s = IN_BROUTER[re];
; #pragma unroll 16
;             for (int j = 0; j < 32; ++j) s += part[(j * 8 + r) * 32 + re];
;             lgb[r * 32 + re] = s; }
.LBB0_828:
	s_or_b64 exec, exec, s[2:3]
	s_and_saveexec_b64 s[98:99], s[8:9]
	global_load_dword v172, v[40:41], off
	s_mov_b64 exec, s[98:99]
	s_add_i32 s16, s90, 8
	s_min_i32 s16, s16, 0x3fff
	s_ashr_i32 s17, s16, 31
	s_lshl_b64 s[100:101], s[16:17], 12
	v_lshl_add_u64 v[170:171], v[36:37], 0, s[100:101]
	global_load_dwordx2 v[122:123], v[170:171], off offset:1536
	global_load_dwordx2 v[124:125], v[170:171], off offset:3584
	global_load_dwordx2 v[126:127], v[170:171], off
	global_load_dwordx2 v[128:129], v[170:171], off offset:512
	global_load_dwordx2 v[130:131], v[170:171], off offset:1024
	global_load_dwordx2 v[132:133], v[170:171], off offset:2048
	global_load_dwordx2 v[134:135], v[170:171], off offset:2560
	global_load_dwordx2 v[136:137], v[170:171], off offset:3072
	s_lshl_b64 s[100:101], s[16:17], 13
	v_lshl_add_u64 v[170:171], v[38:39], 0, s[100:101]
	global_load_dwordx4 v[138:141], v[170:171], off
	global_load_dwordx4 v[142:145], v[170:171], off offset:1024
	global_load_dwordx4 v[146:149], v[170:171], off offset:2048
	global_load_dwordx4 v[150:153], v[170:171], off offset:3072
	s_mov_b32 s100, s92
	s_mov_b32 s101, 0
	v_lshl_add_u64 v[170:171], v[170:171], 0, s[100:101]
	global_load_dwordx4 v[154:157], v[170:171], off
	global_load_dwordx4 v[158:161], v[170:171], off offset:1024
	global_load_dwordx4 v[162:165], v[170:171], off offset:2048
	global_load_dwordx4 v[166:169], v[170:171], off offset:3072
	s_waitcnt lgkmcnt(0)
	s_barrier
	s_and_saveexec_b64 s[2:3], s[8:9]
	s_cbranch_execz .LBB0_832
	s_waitcnt vmcnt(16)
	v_mov_b32_e32 v2, v172
	s_mov_b32 s16, 0
